# speedup vs baseline: 1.0050x; 1.0022x over previous
.LBB0_120:
	s_or_b64 exec, exec, s[4:5]
	v_lshrrev_b32_e32 v1, 6, v0
	v_and_b32_e32 v2, 63, v0
	v_mad_u32_u24 v3, v1, 7, v2
	v_cmp_gt_u32_e32 vcc, 7, v2
	v_cmp_gt_u32_e64 s[4:5], 2, v1
	s_and_b64 s[4:5], s[4:5], vcc
	v_mov_b32_e32 v4, 0xff
	v_cndmask_b32_e64 v3, v4, v3, s[4:5]
	v_lshl_add_u32 v5, v2, 1, 14
	v_cmp_gt_u32_e32 vcc, 2, v2
	v_cmp_eq_u32_e64 s[4:5], 2, v1
	s_and_b64 s[4:5], s[4:5], vcc
	s_nop 1
	v_cndmask_b32_e64 v3, v3, v5, s[4:5]
	v_cmp_eq_u32_e32 vcc, 0xc0, v0
	v_mov_b32_e32 v5, 15
	s_nop 1
	v_cndmask_b32_e32 v0, v3, v5, vcc
	s_cmpk_lt_i32 s2, 0x100
	s_cselect_b64 s[4:5], -1, 0
	v_cmp_gt_u32_e32 vcc, 17, v0
	s_and_b64 s[4:5], s[4:5], vcc
	s_waitcnt lgkmcnt(0)
	s_barrier
	s_and_saveexec_b64 s[6:7], s[4:5]
	s_cbranch_execz .LBB0_151
	v_cmp_lt_u32_e32 vcc, 6, v0
	s_and_saveexec_b64 s[4:5], vcc
	s_xor_b64 s[4:5], exec, s[4:5]
	s_cbranch_execz .LBB0_142
	v_cmp_lt_u32_e32 vcc, 13, v0
	s_and_saveexec_b64 s[6:7], vcc
	s_xor_b64 s[6:7], exec, s[6:7]
	s_cbranch_execz .LBB0_138
	v_mov_b32_e32 v1, 0
	ds_read_b32 v1, v1 offset:64
	s_and_b32 s3, s2, 7
	s_ashr_i32 s14, s2, 3
	v_cmp_lt_i32_e32 vcc, 14, v0
	s_mov_b64 s[10:11], 0
	s_waitcnt lgkmcnt(0)
	v_readfirstlane_b32 s15, v1
	s_and_saveexec_b64 s[8:9], vcc
	s_xor_b64 s[8:9], exec, s[8:9]
	s_cbranch_execz .LBB0_133
	v_cmp_eq_u32_e32 vcc, 15, v0
	s_mov_b64 s[12:13], 0
	s_and_saveexec_b64 s[10:11], vcc
	s_cbranch_execz .LBB0_132
	s_cmp_gt_i32 s15, 64
	s_cbranch_scc0 .LBB0_130
	s_lshl_b32 s12, s15, 5
	s_addk_i32 s12, 0xf800
	s_cmp_lt_i32 s2, s12
	s_cbranch_scc0 .LBB0_129
	s_mul_i32 s12, s3, 22
	s_lshr_b32 s19, s12, 3
	s_add_i32 s12, s12, 22
	s_lshr_b32 s18, s12, 3
	s_lshl_b32 s12, s2, 16
	s_add_i32 s16, s14, 0x100
	s_add_i32 s17, s12, 0x10000
	s_mov_b64 s[12:13], -1
	s_branch .LBB0_131
